# GEMM_A self panels: residual x tile read from the LDS-staged A slot (2 ds_read_b128) instead of 2 global loads per row-group
# baseline (speedup 1.0000x reference)
LgA_setup_self:
	s_sub_u32 s36, s21, 8
	s_lshl_b32 s37, s36, 2
	s_add_u32 s37, s37, s20
	s_lshl_b32 s38, s37, 6
	v_lshlrev_b32_e32 v16, 4, v3
	v_add_u32_e32 v16, s38, v16
	v_lshlrev_b32_e32 v17, 2, v16
	global_load_dwordx4 v[32:35], v17, s[14:15] offset:0
	global_load_dwordx4 v[36:39], v17, s[14:15] offset:16
	global_load_dwordx4 v[40:43], v17, s[14:15] offset:32
	global_load_dwordx4 v[44:47], v17, s[14:15] offset:48
	v_lshlrev_b32_e32 v18, 5, v3
	v_lshl_or_b32 v14, v2, 10, v18
	s_lshl_b32 s39, s23, 14
	s_lshl_b32 s40, s38, 1
	s_add_u32 s39, s39, s40
	s_add_u32 s30, s16, s39
	s_addc_u32 s31, s17, 0
	v_lshl_or_b32 v15, v2, 7, v18
	v_and_b32_e32 v19, 7, v2
	v_lshlrev_b32_e32 v20, 1, v3
	v_xor_b32_e32 v19, v19, v20
	v_lshlrev_b32_e32 v19, 4, v19
	v_lshl_or_b32 v19, v2, 7, v19
	s_lshl_b32 s41, s37, 11
	v_add_u32_e32 v19, s41, v19
	v_sub_u32_e32 v15, v19, v4
	s_mul_i32 s39, s37, 0x140000
	s_lshl_b32 s40, s23, 11
	s_add_u32 s39, s39, s40
	s_add_u32 s32, s4, s39
	s_addc_u32 s33, s5, 0

LgA_self_body:
	v_add_u32_e32 v112, v5, v15
	v_xor_b32_e32 v113, 16, v112
	ds_read_b128 v[80:83], v112
	ds_read_b128 v[84:87], v113
	s_mov_b32 m0, s28
	s_add_u32 s28, s28, 0x4000
	s_cmp_ge_u32 s28, s46
	s_cselect_b32 s28, s47, s28
	global_load_lds_dwordx4 v9, s[26:27]
	global_load_lds_dwordx4 v9, s[26:27] offset:1024
	s_add_u32 m0, m0, 0x800
	s_nop 0
	global_load_lds_dwordx4 v10, s[26:27]
	global_load_lds_dwordx4 v10, s[26:27] offset:1024
	s_add_u32 s26, s26, 0x800
	s_addc_u32 s27, s27, 0
	v_add_u32_e32 v7, s29, v4
	v_xor_b32_e32 v8, 64, v7
	s_add_u32 s29, s29, 0x4000
	s_cmp_ge_u32 s29, 0x14000
	s_cselect_b32 s29, 0, s29
	s_waitcnt vmcnt(63)
	v_mfma_f32_16x16x32_f16 v[48:51], a[0:3], v[128:131], v[32:35]
	v_mfma_f32_16x16x32_f16 v[52:55], a[4:7], v[128:131], v[36:39]
	v_mfma_f32_16x16x32_f16 v[56:59], a[8:11], v[128:131], v[40:43]
	ds_read_b128 v[192:195], v7 offset:0
	v_mfma_f32_16x16x32_f16 v[60:63], a[12:15], v[128:131], v[44:47]
	ds_read_b128 v[196:199], v8 offset:0
	s_waitcnt vmcnt(63)
	v_mfma_f32_16x16x32_f16 v[48:51], a[16:19], v[132:135], v[48:51]
	ds_read_b128 v[200:203], v7 offset:2048
	v_mfma_f32_16x16x32_f16 v[52:55], a[20:23], v[132:135], v[52:55]
	ds_read_b128 v[204:207], v8 offset:2048
	v_mfma_f32_16x16x32_f16 v[56:59], a[24:27], v[132:135], v[56:59]
	ds_read_b128 v[208:211], v7 offset:4096
	v_mfma_f32_16x16x32_f16 v[60:63], a[28:31], v[132:135], v[60:63]
	ds_read_b128 v[212:215], v8 offset:4096
	s_waitcnt vmcnt(63)
	v_mfma_f32_16x16x32_f16 v[48:51], a[32:35], v[136:139], v[48:51]
	ds_read_b128 v[216:219], v7 offset:6144
	v_mfma_f32_16x16x32_f16 v[52:55], a[36:39], v[136:139], v[52:55]
	ds_read_b128 v[220:223], v8 offset:6144
	v_mfma_f32_16x16x32_f16 v[56:59], a[40:43], v[136:139], v[56:59]
	ds_read_b128 v[224:227], v7 offset:8192
	v_mfma_f32_16x16x32_f16 v[60:63], a[44:47], v[136:139], v[60:63]
	ds_read_b128 v[228:231], v8 offset:8192
	s_waitcnt vmcnt(60)
	v_mfma_f32_16x16x32_f16 v[48:51], a[48:51], v[140:143], v[48:51]
	ds_read_b128 v[232:235], v7 offset:10240
	v_mfma_f32_16x16x32_f16 v[52:55], a[52:55], v[140:143], v[52:55]
	ds_read_b128 v[236:239], v8 offset:10240
	v_mfma_f32_16x16x32_f16 v[56:59], a[56:59], v[140:143], v[56:59]
	ds_read_b128 v[240:243], v7 offset:12288
	v_mfma_f32_16x16x32_f16 v[60:63], a[60:63], v[140:143], v[60:63]
	ds_read_b128 v[244:247], v8 offset:12288
	s_waitcnt vmcnt(56)
	v_mfma_f32_16x16x32_f16 v[48:51], a[64:67], v[144:147], v[48:51]
	ds_read_b128 v[248:251], v7 offset:14336
	v_mfma_f32_16x16x32_f16 v[52:55], a[68:71], v[144:147], v[52:55]
	ds_read_b128 v[252:255], v8 offset:14336
	v_mfma_f32_16x16x32_f16 v[56:59], a[72:75], v[144:147], v[56:59]
	v_mfma_f32_16x16x32_f16 v[60:63], a[76:79], v[144:147], v[60:63]
	s_waitcnt vmcnt(52)
	v_mfma_f32_16x16x32_f16 v[48:51], a[80:83], v[148:151], v[48:51]
	v_mfma_f32_16x16x32_f16 v[52:55], a[84:87], v[148:151], v[52:55]
	v_mfma_f32_16x16x32_f16 v[56:59], a[88:91], v[148:151], v[56:59]
	v_mfma_f32_16x16x32_f16 v[60:63], a[92:95], v[148:151], v[60:63]
	s_waitcnt vmcnt(48)
	v_mfma_f32_16x16x32_f16 v[48:51], a[96:99], v[152:155], v[48:51]
	v_mfma_f32_16x16x32_f16 v[52:55], a[100:103], v[152:155], v[52:55]
	v_mfma_f32_16x16x32_f16 v[56:59], a[104:107], v[152:155], v[56:59]
	v_mfma_f32_16x16x32_f16 v[60:63], a[108:111], v[152:155], v[60:63]
	s_waitcnt vmcnt(44)
	v_mfma_f32_16x16x32_f16 v[48:51], a[112:115], v[156:159], v[48:51]
	v_mfma_f32_16x16x32_f16 v[52:55], a[116:119], v[156:159], v[52:55]
	v_mfma_f32_16x16x32_f16 v[56:59], a[120:123], v[156:159], v[56:59]
	v_mfma_f32_16x16x32_f16 v[60:63], a[124:127], v[156:159], v[60:63]
	s_waitcnt vmcnt(40)
	v_mfma_f32_16x16x32_f16 v[48:51], a[128:131], v[160:163], v[48:51]
	v_mfma_f32_16x16x32_f16 v[52:55], a[132:135], v[160:163], v[52:55]
	v_mfma_f32_16x16x32_f16 v[56:59], a[136:139], v[160:163], v[56:59]
	v_mfma_f32_16x16x32_f16 v[60:63], a[140:143], v[160:163], v[60:63]
	s_waitcnt vmcnt(36)
	v_mfma_f32_16x16x32_f16 v[48:51], a[144:147], v[164:167], v[48:51]
	v_mfma_f32_16x16x32_f16 v[52:55], a[148:151], v[164:167], v[52:55]
	v_mfma_f32_16x16x32_f16 v[56:59], a[152:155], v[164:167], v[56:59]
	v_mfma_f32_16x16x32_f16 v[60:63], a[156:159], v[164:167], v[60:63]
	s_waitcnt vmcnt(32)
	v_mfma_f32_16x16x32_f16 v[48:51], a[160:163], v[168:171], v[48:51]
	v_mfma_f32_16x16x32_f16 v[52:55], a[164:167], v[168:171], v[52:55]
	v_mfma_f32_16x16x32_f16 v[56:59], a[168:171], v[168:171], v[56:59]
	v_mfma_f32_16x16x32_f16 v[60:63], a[172:175], v[168:171], v[60:63]
	s_waitcnt vmcnt(28)
	v_mfma_f32_16x16x32_f16 v[48:51], a[176:179], v[172:175], v[48:51]
	v_mfma_f32_16x16x32_f16 v[52:55], a[180:183], v[172:175], v[52:55]
	v_mfma_f32_16x16x32_f16 v[56:59], a[184:187], v[172:175], v[56:59]
	v_mfma_f32_16x16x32_f16 v[60:63], a[188:191], v[172:175], v[60:63]
	s_waitcnt vmcnt(24)
	v_mfma_f32_16x16x32_f16 v[48:51], a[192:195], v[176:179], v[48:51]
	v_mfma_f32_16x16x32_f16 v[52:55], a[196:199], v[176:179], v[52:55]
	v_mfma_f32_16x16x32_f16 v[56:59], a[200:203], v[176:179], v[56:59]
	v_mfma_f32_16x16x32_f16 v[60:63], a[204:207], v[176:179], v[60:63]
	s_waitcnt vmcnt(20)
	v_mfma_f32_16x16x32_f16 v[48:51], a[208:211], v[180:183], v[48:51]
	v_mfma_f32_16x16x32_f16 v[52:55], a[212:215], v[180:183], v[52:55]
	v_mfma_f32_16x16x32_f16 v[56:59], a[216:219], v[180:183], v[56:59]
	v_mfma_f32_16x16x32_f16 v[60:63], a[220:223], v[180:183], v[60:63]
	s_waitcnt vmcnt(16)
	v_mfma_f32_16x16x32_f16 v[48:51], a[224:227], v[184:187], v[48:51]
	v_mfma_f32_16x16x32_f16 v[52:55], a[228:231], v[184:187], v[52:55]
	v_mfma_f32_16x16x32_f16 v[56:59], a[232:235], v[184:187], v[56:59]
	v_mfma_f32_16x16x32_f16 v[60:63], a[236:239], v[184:187], v[60:63]
	s_waitcnt vmcnt(12)
	v_mfma_f32_16x16x32_f16 v[48:51], a[240:243], v[188:191], v[48:51]
	v_mfma_f32_16x16x32_f16 v[52:55], a[244:247], v[188:191], v[52:55]
	v_mfma_f32_16x16x32_f16 v[56:59], a[248:251], v[188:191], v[56:59]
	v_mfma_f32_16x16x32_f16 v[60:63], a[252:255], v[188:191], v[60:63]
LgAs_loop:
	s_waitcnt vmcnt(8) lgkmcnt(0)
	s_barrier
	v_mfma_f32_16x16x32_f16 v[64:67], a[0:3], v[192:195], v[32:35]
	v_add_u32_e32 v112, v7, v15
	v_xor_b32_e32 v113, 16, v112
	ds_read_b128 v[88:91], v112
	ds_read_b128 v[92:95], v113
	v_mfma_f32_16x16x32_f16 v[68:71], a[4:7], v[192:195], v[36:39]
	v_add_u32_e32 v5, s29, v4
	v_xor_b32_e32 v6, 64, v5
	s_add_u32 s29, s29, 0x4000
	s_cmp_ge_u32 s29, 0x14000
	s_cselect_b32 s29, 0, s29
	v_mfma_f32_16x16x32_f16 v[72:75], a[8:11], v[192:195], v[40:43]
	ds_read_b128 v[128:131], v5 offset:0
	v_mfma_f32_16x16x32_f16 v[76:79], a[12:15], v[192:195], v[44:47]
	ds_read_b128 v[132:135], v6 offset:0
	v_cvt_f32_f16_e32 v96, v80
	v_mfma_f32_16x16x32_f16 v[64:67], a[16:19], v[196:199], v[64:67]
	ds_read_b128 v[136:139], v5 offset:2048
	v_cvt_f32_f16_sdwa v97, v80 dst_sel:DWORD dst_unused:UNUSED_PAD src0_sel:WORD_1
	v_mfma_f32_16x16x32_f16 v[68:71], a[20:23], v[196:199], v[68:71]
	ds_read_b128 v[140:143], v6 offset:2048
	v_cvt_f32_f16_e32 v98, v81
	v_mfma_f32_16x16x32_f16 v[72:75], a[24:27], v[196:199], v[72:75]
	ds_read_b128 v[144:147], v5 offset:4096
	v_mfma_f32_16x16x32_f16 v[76:79], a[28:31], v[196:199], v[76:79]
	ds_read_b128 v[148:151], v6 offset:4096
	v_cvt_f32_f16_sdwa v99, v81 dst_sel:DWORD dst_unused:UNUSED_PAD src0_sel:WORD_1
	v_mfma_f32_16x16x32_f16 v[64:67], a[32:35], v[200:203], v[64:67]
	ds_read_b128 v[152:155], v5 offset:6144
	v_cvt_f32_f16_e32 v100, v82
	v_mfma_f32_16x16x32_f16 v[68:71], a[36:39], v[200:203], v[68:71]
	ds_read_b128 v[156:159], v6 offset:6144
	v_cvt_f32_f16_sdwa v101, v82 dst_sel:DWORD dst_unused:UNUSED_PAD src0_sel:WORD_1
	v_mfma_f32_16x16x32_f16 v[72:75], a[40:43], v[200:203], v[72:75]
	ds_read_b128 v[160:163], v5 offset:8192
	v_mfma_f32_16x16x32_f16 v[76:79], a[44:47], v[200:203], v[76:79]
	ds_read_b128 v[164:167], v6 offset:8192
	v_cvt_f32_f16_e32 v102, v83
	v_mfma_f32_16x16x32_f16 v[64:67], a[48:51], v[204:207], v[64:67]
	ds_read_b128 v[168:171], v5 offset:10240
	v_cvt_f32_f16_sdwa v103, v83 dst_sel:DWORD dst_unused:UNUSED_PAD src0_sel:WORD_1
	v_mfma_f32_16x16x32_f16 v[68:71], a[52:55], v[204:207], v[68:71]
	ds_read_b128 v[172:175], v6 offset:10240
	v_cvt_f32_f16_e32 v104, v84
	v_mfma_f32_16x16x32_f16 v[72:75], a[56:59], v[204:207], v[72:75]
	ds_read_b128 v[176:179], v5 offset:12288
	v_mfma_f32_16x16x32_f16 v[76:79], a[60:63], v[204:207], v[76:79]
	ds_read_b128 v[180:183], v6 offset:12288
	v_cvt_f32_f16_sdwa v105, v84 dst_sel:DWORD dst_unused:UNUSED_PAD src0_sel:WORD_1
	v_mfma_f32_16x16x32_f16 v[64:67], a[64:67], v[208:211], v[64:67]
	ds_read_b128 v[184:187], v5 offset:14336
	v_cvt_f32_f16_e32 v106, v85
	v_mfma_f32_16x16x32_f16 v[68:71], a[68:71], v[208:211], v[68:71]
	ds_read_b128 v[188:191], v6 offset:14336
	v_cvt_f32_f16_sdwa v107, v85 dst_sel:DWORD dst_unused:UNUSED_PAD src0_sel:WORD_1
	v_mfma_f32_16x16x32_f16 v[72:75], a[72:75], v[208:211], v[72:75]
	v_mfma_f32_16x16x32_f16 v[76:79], a[76:79], v[208:211], v[76:79]
	v_cvt_f32_f16_e32 v108, v86
	v_mfma_f32_16x16x32_f16 v[64:67], a[80:83], v[212:215], v[64:67]
	v_cvt_f32_f16_sdwa v109, v86 dst_sel:DWORD dst_unused:UNUSED_PAD src0_sel:WORD_1
	v_mfma_f32_16x16x32_f16 v[68:71], a[84:87], v[212:215], v[68:71]
	v_cvt_f32_f16_e32 v110, v87
	v_mfma_f32_16x16x32_f16 v[72:75], a[88:91], v[212:215], v[72:75]
	s_mov_b32 m0, s28
	s_add_u32 s28, s28, 0x4000
	s_cmp_ge_u32 s28, s46
	s_cselect_b32 s28, s47, s28
	global_load_lds_dwordx4 v9, s[26:27]
	v_mfma_f32_16x16x32_f16 v[76:79], a[92:95], v[212:215], v[76:79]
	v_cvt_f32_f16_sdwa v111, v87 dst_sel:DWORD dst_unused:UNUSED_PAD src0_sel:WORD_1
	v_mfma_f32_16x16x32_f16 v[64:67], a[96:99], v[216:219], v[64:67]
	v_add_f32_e32 v96, v96, v48
	v_mfma_f32_16x16x32_f16 v[68:71], a[100:103], v[216:219], v[68:71]
	v_add_f32_e32 v97, v97, v49
	v_mfma_f32_16x16x32_f16 v[72:75], a[104:107], v[216:219], v[72:75]
	v_mfma_f32_16x16x32_f16 v[76:79], a[108:111], v[216:219], v[76:79]
	v_add_f32_e32 v98, v98, v50
	v_mfma_f32_16x16x32_f16 v[64:67], a[112:115], v[220:223], v[64:67]
	v_add_f32_e32 v99, v99, v51
	v_mfma_f32_16x16x32_f16 v[68:71], a[116:119], v[220:223], v[68:71]
	v_add_f32_e32 v100, v100, v52
	v_mfma_f32_16x16x32_f16 v[72:75], a[120:123], v[220:223], v[72:75]
	v_mfma_f32_16x16x32_f16 v[76:79], a[124:127], v[220:223], v[76:79]
	v_add_f32_e32 v101, v101, v53
	v_mfma_f32_16x16x32_f16 v[64:67], a[128:131], v[224:227], v[64:67]
	v_add_f32_e32 v102, v102, v54
	v_mfma_f32_16x16x32_f16 v[68:71], a[132:135], v[224:227], v[68:71]
	global_load_lds_dwordx4 v9, s[26:27] offset:1024
	v_add_f32_e32 v103, v103, v55
	v_mfma_f32_16x16x32_f16 v[72:75], a[136:139], v[224:227], v[72:75]
	v_mfma_f32_16x16x32_f16 v[76:79], a[140:143], v[224:227], v[76:79]
	v_add_f32_e32 v104, v104, v56
	v_mfma_f32_16x16x32_f16 v[64:67], a[144:147], v[228:231], v[64:67]
	v_add_f32_e32 v105, v105, v57
	v_mfma_f32_16x16x32_f16 v[68:71], a[148:151], v[228:231], v[68:71]
	v_add_f32_e32 v106, v106, v58
	v_mfma_f32_16x16x32_f16 v[72:75], a[152:155], v[228:231], v[72:75]
	v_mfma_f32_16x16x32_f16 v[76:79], a[156:159], v[228:231], v[76:79]
	v_add_f32_e32 v107, v107, v59
	v_mfma_f32_16x16x32_f16 v[64:67], a[160:163], v[232:235], v[64:67]
	v_add_f32_e32 v108, v108, v60
	v_mfma_f32_16x16x32_f16 v[68:71], a[164:167], v[232:235], v[68:71]
	v_add_f32_e32 v109, v109, v61
	v_mfma_f32_16x16x32_f16 v[72:75], a[168:171], v[232:235], v[72:75]
	v_mfma_f32_16x16x32_f16 v[76:79], a[172:175], v[232:235], v[76:79]
	v_add_f32_e32 v110, v110, v62
	v_mfma_f32_16x16x32_f16 v[64:67], a[176:179], v[236:239], v[64:67]
	s_add_u32 m0, m0, 0x800
	s_nop 0
	global_load_lds_dwordx4 v10, s[26:27]
	v_add_f32_e32 v111, v111, v63
	v_mfma_f32_16x16x32_f16 v[68:71], a[180:183], v[236:239], v[68:71]
	v_cvt_pk_f16_f32 v16, v96, v97
	v_mfma_f32_16x16x32_f16 v[72:75], a[184:187], v[236:239], v[72:75]
	v_mfma_f32_16x16x32_f16 v[76:79], a[188:191], v[236:239], v[76:79]
	v_cvt_pk_f16_f32 v17, v98, v99
	v_mfma_f32_16x16x32_f16 v[64:67], a[192:195], v[240:243], v[64:67]
	v_cvt_pk_f16_f32 v18, v100, v101
	v_mfma_f32_16x16x32_f16 v[68:71], a[196:199], v[240:243], v[68:71]
	v_cvt_pk_f16_f32 v19, v102, v103
	v_mfma_f32_16x16x32_f16 v[72:75], a[200:203], v[240:243], v[72:75]
	v_mfma_f32_16x16x32_f16 v[76:79], a[204:207], v[240:243], v[76:79]
	v_cvt_pk_f16_f32 v20, v104, v105
	v_mfma_f32_16x16x32_f16 v[64:67], a[208:211], v[244:247], v[64:67]
	v_cvt_pk_f16_f32 v21, v106, v107
	v_mfma_f32_16x16x32_f16 v[68:71], a[212:215], v[244:247], v[68:71]
	v_cvt_pk_f16_f32 v22, v108, v109
	v_mfma_f32_16x16x32_f16 v[72:75], a[216:219], v[244:247], v[72:75]
	v_mfma_f32_16x16x32_f16 v[76:79], a[220:223], v[244:247], v[76:79]
	v_cvt_pk_f16_f32 v23, v110, v111
	v_mfma_f32_16x16x32_f16 v[64:67], a[224:227], v[248:251], v[64:67]
	global_load_lds_dwordx4 v10, s[26:27] offset:1024
	global_store_dwordx4 v14, v[16:19], s[30:31]
	v_mfma_f32_16x16x32_f16 v[68:71], a[228:231], v[248:251], v[68:71]
	s_add_u32 s26, s26, 0x800
	s_addc_u32 s27, s27, 0
	global_store_dwordx4 v14, v[20:23], s[30:31] offset:16
	v_mfma_f32_16x16x32_f16 v[72:75], a[232:235], v[248:251], v[72:75]
	v_mfma_f32_16x16x32_f16 v[76:79], a[236:239], v[248:251], v[76:79]
	s_add_u32 s30, s30, 0x4000
	s_addc_u32 s31, s31, 0
	v_mfma_f32_16x16x32_f16 v[64:67], a[240:243], v[252:255], v[64:67]
	v_mfma_f32_16x16x32_f16 v[68:71], a[244:247], v[252:255], v[68:71]
	v_mfma_f32_16x16x32_f16 v[72:75], a[248:251], v[252:255], v[72:75]
	v_mfma_f32_16x16x32_f16 v[76:79], a[252:255], v[252:255], v[76:79]
	s_sub_u32 s24, s24, 1
	s_cmp_le_u32 s24, 1
	s_cbranch_scc1 LgAs_exitA
	s_waitcnt vmcnt(8) lgkmcnt(0)
	s_barrier
	v_mfma_f32_16x16x32_f16 v[48:51], a[0:3], v[128:131], v[32:35]
	v_add_u32_e32 v112, v5, v15
	v_xor_b32_e32 v113, 16, v112
	ds_read_b128 v[80:83], v112
	ds_read_b128 v[84:87], v113
	v_mfma_f32_16x16x32_f16 v[52:55], a[4:7], v[128:131], v[36:39]
	v_add_u32_e32 v7, s29, v4
	v_xor_b32_e32 v8, 64, v7
	s_add_u32 s29, s29, 0x4000
	s_cmp_ge_u32 s29, 0x14000
	s_cselect_b32 s29, 0, s29
	v_mfma_f32_16x16x32_f16 v[56:59], a[8:11], v[128:131], v[40:43]
	ds_read_b128 v[192:195], v7 offset:0
	v_mfma_f32_16x16x32_f16 v[60:63], a[12:15], v[128:131], v[44:47]
	ds_read_b128 v[196:199], v8 offset:0
	v_cvt_f32_f16_e32 v96, v88
	v_mfma_f32_16x16x32_f16 v[48:51], a[16:19], v[132:135], v[48:51]
	ds_read_b128 v[200:203], v7 offset:2048
	v_cvt_f32_f16_sdwa v97, v88 dst_sel:DWORD dst_unused:UNUSED_PAD src0_sel:WORD_1
	v_mfma_f32_16x16x32_f16 v[52:55], a[20:23], v[132:135], v[52:55]
	ds_read_b128 v[204:207], v8 offset:2048
	v_cvt_f32_f16_e32 v98, v89
	v_mfma_f32_16x16x32_f16 v[56:59], a[24:27], v[132:135], v[56:59]
	ds_read_b128 v[208:211], v7 offset:4096
	v_mfma_f32_16x16x32_f16 v[60:63], a[28:31], v[132:135], v[60:63]
	ds_read_b128 v[212:215], v8 offset:4096
	v_cvt_f32_f16_sdwa v99, v89 dst_sel:DWORD dst_unused:UNUSED_PAD src0_sel:WORD_1
	v_mfma_f32_16x16x32_f16 v[48:51], a[32:35], v[136:139], v[48:51]
	ds_read_b128 v[216:219], v7 offset:6144
	v_cvt_f32_f16_e32 v100, v90
	v_mfma_f32_16x16x32_f16 v[52:55], a[36:39], v[136:139], v[52:55]
	ds_read_b128 v[220:223], v8 offset:6144
	v_cvt_f32_f16_sdwa v101, v90 dst_sel:DWORD dst_unused:UNUSED_PAD src0_sel:WORD_1
	v_mfma_f32_16x16x32_f16 v[56:59], a[40:43], v[136:139], v[56:59]
	ds_read_b128 v[224:227], v7 offset:8192
	v_mfma_f32_16x16x32_f16 v[60:63], a[44:47], v[136:139], v[60:63]
	ds_read_b128 v[228:231], v8 offset:8192
	v_cvt_f32_f16_e32 v102, v91
	v_mfma_f32_16x16x32_f16 v[48:51], a[48:51], v[140:143], v[48:51]
	ds_read_b128 v[232:235], v7 offset:10240
	v_cvt_f32_f16_sdwa v103, v91 dst_sel:DWORD dst_unused:UNUSED_PAD src0_sel:WORD_1
	v_mfma_f32_16x16x32_f16 v[52:55], a[52:55], v[140:143], v[52:55]
	ds_read_b128 v[236:239], v8 offset:10240
	v_cvt_f32_f16_e32 v104, v92
	v_mfma_f32_16x16x32_f16 v[56:59], a[56:59], v[140:143], v[56:59]
	ds_read_b128 v[240:243], v7 offset:12288
	v_mfma_f32_16x16x32_f16 v[60:63], a[60:63], v[140:143], v[60:63]
	ds_read_b128 v[244:247], v8 offset:12288
	v_cvt_f32_f16_sdwa v105, v92 dst_sel:DWORD dst_unused:UNUSED_PAD src0_sel:WORD_1
	v_mfma_f32_16x16x32_f16 v[48:51], a[64:67], v[144:147], v[48:51]
	ds_read_b128 v[248:251], v7 offset:14336
	v_cvt_f32_f16_e32 v106, v93
	v_mfma_f32_16x16x32_f16 v[52:55], a[68:71], v[144:147], v[52:55]
	ds_read_b128 v[252:255], v8 offset:14336
	v_cvt_f32_f16_sdwa v107, v93 dst_sel:DWORD dst_unused:UNUSED_PAD src0_sel:WORD_1
	v_mfma_f32_16x16x32_f16 v[56:59], a[72:75], v[144:147], v[56:59]
	v_mfma_f32_16x16x32_f16 v[60:63], a[76:79], v[144:147], v[60:63]
	v_cvt_f32_f16_e32 v108, v94
	v_mfma_f32_16x16x32_f16 v[48:51], a[80:83], v[148:151], v[48:51]
	v_cvt_f32_f16_sdwa v109, v94 dst_sel:DWORD dst_unused:UNUSED_PAD src0_sel:WORD_1
	v_mfma_f32_16x16x32_f16 v[52:55], a[84:87], v[148:151], v[52:55]
	v_cvt_f32_f16_e32 v110, v95
	v_mfma_f32_16x16x32_f16 v[56:59], a[88:91], v[148:151], v[56:59]
	s_mov_b32 m0, s28
	s_add_u32 s28, s28, 0x4000
	s_cmp_ge_u32 s28, s46
	s_cselect_b32 s28, s47, s28
	global_load_lds_dwordx4 v9, s[26:27]
	v_mfma_f32_16x16x32_f16 v[60:63], a[92:95], v[148:151], v[60:63]
	v_cvt_f32_f16_sdwa v111, v95 dst_sel:DWORD dst_unused:UNUSED_PAD src0_sel:WORD_1
	v_mfma_f32_16x16x32_f16 v[48:51], a[96:99], v[152:155], v[48:51]
	v_add_f32_e32 v96, v96, v64
	v_mfma_f32_16x16x32_f16 v[52:55], a[100:103], v[152:155], v[52:55]
	v_add_f32_e32 v97, v97, v65
	v_mfma_f32_16x16x32_f16 v[56:59], a[104:107], v[152:155], v[56:59]
	v_mfma_f32_16x16x32_f16 v[60:63], a[108:111], v[152:155], v[60:63]
	v_add_f32_e32 v98, v98, v66
	v_mfma_f32_16x16x32_f16 v[48:51], a[112:115], v[156:159], v[48:51]
	v_add_f32_e32 v99, v99, v67
	v_mfma_f32_16x16x32_f16 v[52:55], a[116:119], v[156:159], v[52:55]
	v_add_f32_e32 v100, v100, v68
	v_mfma_f32_16x16x32_f16 v[56:59], a[120:123], v[156:159], v[56:59]
	v_mfma_f32_16x16x32_f16 v[60:63], a[124:127], v[156:159], v[60:63]
	v_add_f32_e32 v101, v101, v69
	v_mfma_f32_16x16x32_f16 v[48:51], a[128:131], v[160:163], v[48:51]
	v_add_f32_e32 v102, v102, v70
	v_mfma_f32_16x16x32_f16 v[52:55], a[132:135], v[160:163], v[52:55]
	global_load_lds_dwordx4 v9, s[26:27] offset:1024
	v_add_f32_e32 v103, v103, v71
	v_mfma_f32_16x16x32_f16 v[56:59], a[136:139], v[160:163], v[56:59]
	v_mfma_f32_16x16x32_f16 v[60:63], a[140:143], v[160:163], v[60:63]
	v_add_f32_e32 v104, v104, v72
	v_mfma_f32_16x16x32_f16 v[48:51], a[144:147], v[164:167], v[48:51]
	v_add_f32_e32 v105, v105, v73
	v_mfma_f32_16x16x32_f16 v[52:55], a[148:151], v[164:167], v[52:55]
	v_add_f32_e32 v106, v106, v74
	v_mfma_f32_16x16x32_f16 v[56:59], a[152:155], v[164:167], v[56:59]
	v_mfma_f32_16x16x32_f16 v[60:63], a[156:159], v[164:167], v[60:63]
	v_add_f32_e32 v107, v107, v75
	v_mfma_f32_16x16x32_f16 v[48:51], a[160:163], v[168:171], v[48:51]
	v_add_f32_e32 v108, v108, v76
	v_mfma_f32_16x16x32_f16 v[52:55], a[164:167], v[168:171], v[52:55]
	v_add_f32_e32 v109, v109, v77
	v_mfma_f32_16x16x32_f16 v[56:59], a[168:171], v[168:171], v[56:59]
	v_mfma_f32_16x16x32_f16 v[60:63], a[172:175], v[168:171], v[60:63]
	v_add_f32_e32 v110, v110, v78
	v_mfma_f32_16x16x32_f16 v[48:51], a[176:179], v[172:175], v[48:51]
	s_add_u32 m0, m0, 0x800
	s_nop 0
	global_load_lds_dwordx4 v10, s[26:27]
	v_add_f32_e32 v111, v111, v79
	v_mfma_f32_16x16x32_f16 v[52:55], a[180:183], v[172:175], v[52:55]
	v_cvt_pk_f16_f32 v16, v96, v97
	v_mfma_f32_16x16x32_f16 v[56:59], a[184:187], v[172:175], v[56:59]
	v_mfma_f32_16x16x32_f16 v[60:63], a[188:191], v[172:175], v[60:63]
	v_cvt_pk_f16_f32 v17, v98, v99
	v_mfma_f32_16x16x32_f16 v[48:51], a[192:195], v[176:179], v[48:51]
	v_cvt_pk_f16_f32 v18, v100, v101
	v_mfma_f32_16x16x32_f16 v[52:55], a[196:199], v[176:179], v[52:55]
	v_cvt_pk_f16_f32 v19, v102, v103
	v_mfma_f32_16x16x32_f16 v[56:59], a[200:203], v[176:179], v[56:59]
	v_mfma_f32_16x16x32_f16 v[60:63], a[204:207], v[176:179], v[60:63]
	v_cvt_pk_f16_f32 v20, v104, v105
	v_mfma_f32_16x16x32_f16 v[48:51], a[208:211], v[180:183], v[48:51]
	v_cvt_pk_f16_f32 v21, v106, v107
	v_mfma_f32_16x16x32_f16 v[52:55], a[212:215], v[180:183], v[52:55]
	v_cvt_pk_f16_f32 v22, v108, v109
	v_mfma_f32_16x16x32_f16 v[56:59], a[216:219], v[180:183], v[56:59]
	v_mfma_f32_16x16x32_f16 v[60:63], a[220:223], v[180:183], v[60:63]
	v_cvt_pk_f16_f32 v23, v110, v111
	v_mfma_f32_16x16x32_f16 v[48:51], a[224:227], v[184:187], v[48:51]
	global_load_lds_dwordx4 v10, s[26:27] offset:1024
	global_store_dwordx4 v14, v[16:19], s[30:31]
	v_mfma_f32_16x16x32_f16 v[52:55], a[228:231], v[184:187], v[52:55]
	s_add_u32 s26, s26, 0x800
	s_addc_u32 s27, s27, 0
	global_store_dwordx4 v14, v[20:23], s[30:31] offset:16
	v_mfma_f32_16x16x32_f16 v[56:59], a[232:235], v[184:187], v[56:59]
	v_mfma_f32_16x16x32_f16 v[60:63], a[236:239], v[184:187], v[60:63]
	s_add_u32 s30, s30, 0x4000
	s_addc_u32 s31, s31, 0
	v_mfma_f32_16x16x32_f16 v[48:51], a[240:243], v[188:191], v[48:51]
	v_mfma_f32_16x16x32_f16 v[52:55], a[244:247], v[188:191], v[52:55]
	v_mfma_f32_16x16x32_f16 v[56:59], a[248:251], v[188:191], v[56:59]
	v_mfma_f32_16x16x32_f16 v[60:63], a[252:255], v[188:191], v[60:63]
	s_sub_u32 s24, s24, 1
	s_cmp_le_u32 s24, 1
	s_cbranch_scc0 LgAs_loop
	s_nop 7
	s_nop 7
	s_waitcnt vmcnt(0) lgkmcnt(0)
	v_cvt_f32_f16_e32 v96, v80
	v_cvt_f32_f16_sdwa v97, v80 dst_sel:DWORD dst_unused:UNUSED_PAD src0_sel:WORD_1
	v_cvt_f32_f16_e32 v98, v81
	v_cvt_f32_f16_sdwa v99, v81 dst_sel:DWORD dst_unused:UNUSED_PAD src0_sel:WORD_1
	v_cvt_f32_f16_e32 v100, v82
	v_cvt_f32_f16_sdwa v101, v82 dst_sel:DWORD dst_unused:UNUSED_PAD src0_sel:WORD_1
	v_cvt_f32_f16_e32 v102, v83
	v_cvt_f32_f16_sdwa v103, v83 dst_sel:DWORD dst_unused:UNUSED_PAD src0_sel:WORD_1
	v_cvt_f32_f16_e32 v104, v84
	v_cvt_f32_f16_sdwa v105, v84 dst_sel:DWORD dst_unused:UNUSED_PAD src0_sel:WORD_1
	v_cvt_f32_f16_e32 v106, v85
	v_cvt_f32_f16_sdwa v107, v85 dst_sel:DWORD dst_unused:UNUSED_PAD src0_sel:WORD_1
	v_cvt_f32_f16_e32 v108, v86
	v_cvt_f32_f16_sdwa v109, v86 dst_sel:DWORD dst_unused:UNUSED_PAD src0_sel:WORD_1
	v_cvt_f32_f16_e32 v110, v87
	v_cvt_f32_f16_sdwa v111, v87 dst_sel:DWORD dst_unused:UNUSED_PAD src0_sel:WORD_1
	v_add_f32_e32 v96, v96, v48
	v_add_f32_e32 v97, v97, v49
	v_add_f32_e32 v98, v98, v50
	v_add_f32_e32 v99, v99, v51
	v_add_f32_e32 v100, v100, v52
	v_add_f32_e32 v101, v101, v53
	v_add_f32_e32 v102, v102, v54
	v_add_f32_e32 v103, v103, v55
	v_add_f32_e32 v104, v104, v56
	v_add_f32_e32 v105, v105, v57
	v_add_f32_e32 v106, v106, v58
	v_add_f32_e32 v107, v107, v59
	v_add_f32_e32 v108, v108, v60
	v_add_f32_e32 v109, v109, v61
	v_add_f32_e32 v110, v110, v62
	v_add_f32_e32 v111, v111, v63
	v_cvt_pk_f16_f32 v16, v96, v97
	v_cvt_pk_f16_f32 v17, v98, v99
	v_cvt_pk_f16_f32 v18, v100, v101
	v_cvt_pk_f16_f32 v19, v102, v103
	v_cvt_pk_f16_f32 v20, v104, v105
	v_cvt_pk_f16_f32 v21, v106, v107
	v_cvt_pk_f16_f32 v22, v108, v109
	v_cvt_pk_f16_f32 v23, v110, v111
	global_store_dwordx4 v14, v[16:19], s[30:31]
	global_store_dwordx4 v14, v[20:23], s[30:31] offset:16
	s_add_u32 s30, s30, 0x4000
	s_addc_u32 s31, s31, 0
	s_endpgm
LgAs_exitA:
	s_nop 7
	s_nop 7
	s_waitcnt vmcnt(0) lgkmcnt(0)
	v_cvt_f32_f16_e32 v96, v88
	v_cvt_f32_f16_sdwa v97, v88 dst_sel:DWORD dst_unused:UNUSED_PAD src0_sel:WORD_1
	v_cvt_f32_f16_e32 v98, v89
	v_cvt_f32_f16_sdwa v99, v89 dst_sel:DWORD dst_unused:UNUSED_PAD src0_sel:WORD_1
	v_cvt_f32_f16_e32 v100, v90
	v_cvt_f32_f16_sdwa v101, v90 dst_sel:DWORD dst_unused:UNUSED_PAD src0_sel:WORD_1
	v_cvt_f32_f16_e32 v102, v91
	v_cvt_f32_f16_sdwa v103, v91 dst_sel:DWORD dst_unused:UNUSED_PAD src0_sel:WORD_1
	v_cvt_f32_f16_e32 v104, v92
	v_cvt_f32_f16_sdwa v105, v92 dst_sel:DWORD dst_unused:UNUSED_PAD src0_sel:WORD_1
	v_cvt_f32_f16_e32 v106, v93
	v_cvt_f32_f16_sdwa v107, v93 dst_sel:DWORD dst_unused:UNUSED_PAD src0_sel:WORD_1
	v_cvt_f32_f16_e32 v108, v94
	v_cvt_f32_f16_sdwa v109, v94 dst_sel:DWORD dst_unused:UNUSED_PAD src0_sel:WORD_1
	v_cvt_f32_f16_e32 v110, v95
	v_cvt_f32_f16_sdwa v111, v95 dst_sel:DWORD dst_unused:UNUSED_PAD src0_sel:WORD_1
	v_add_f32_e32 v96, v96, v64
	v_add_f32_e32 v97, v97, v65
	v_add_f32_e32 v98, v98, v66
	v_add_f32_e32 v99, v99, v67
	v_add_f32_e32 v100, v100, v68
	v_add_f32_e32 v101, v101, v69
	v_add_f32_e32 v102, v102, v70
	v_add_f32_e32 v103, v103, v71
	v_add_f32_e32 v104, v104, v72
	v_add_f32_e32 v105, v105, v73
	v_add_f32_e32 v106, v106, v74
	v_add_f32_e32 v107, v107, v75
	v_add_f32_e32 v108, v108, v76
	v_add_f32_e32 v109, v109, v77
	v_add_f32_e32 v110, v110, v78
	v_add_f32_e32 v111, v111, v79
	v_cvt_pk_f16_f32 v16, v96, v97
	v_cvt_pk_f16_f32 v17, v98, v99
	v_cvt_pk_f16_f32 v18, v100, v101
	v_cvt_pk_f16_f32 v19, v102, v103
	v_cvt_pk_f16_f32 v20, v104, v105
	v_cvt_pk_f16_f32 v21, v106, v107
	v_cvt_pk_f16_f32 v22, v108, v109
	v_cvt_pk_f16_f32 v23, v110, v111
	global_store_dwordx4 v14, v[16:19], s[30:31]
	global_store_dwordx4 v14, v[20:23], s[30:31] offset:16
	s_add_u32 s30, s30, 0x4000
	s_addc_u32 s31, s31, 0
	s_endpgm
